# batch 3 plus an early L2 write-back (buffer_wbl2) issued by wave 0 of every workgroup as it arrives at each grid barrier
# speedup vs baseline: 1.0132x; 1.0132x over previous
; __device__ __forceinline__ unsigned xb_ld(unsigned* p)              { return __hip_atomic_load(p, __ATOMIC_RELAXED, __HIP_MEMORY_SCOPE_AGENT); }
; __device__ __forceinline__ unsigned xb_add(unsigned* p, unsigned v) { return __hip_atomic_fetch_add(p, v, __ATOMIC_RELAXED, __HIP_MEMORY_SCOPE_AGENT); }
; __device__ __forceinline__ void xcd_barrier_complete(unsigned* bar, unsigned x, unsigned& nloc, unsigned& nx) {
;     const unsigned G = gridDim.x * gridDim.y * gridDim.z;
;     unsigned sum, cnt, mine, sp = 0u;
;     for (;;) {
;         sum = 0u; cnt = 0u; mine = 0u;
; #pragma unroll
;         for (unsigned j = 0; j < 16; ++j) { const unsigned c = xb_ld(&bar[XB_XCNT(j)]); sum += c; cnt += (c > 0u) ? 1u : 0u; mine = (j == x) ? c : mine; }
; __device__ __forceinline__ void xcd_barrier(const XcdBarrier& b, bool t0) {
;     asm volatile("s_waitcnt vmcnt(0)" ::: "memory");
;     __syncthreads();
;     if (t0) {
;         unsigned* bar = b.bar;
;         __builtin_amdgcn_s_waitcnt(0);
;         unsigned nloc = b.st[0], nx = b.st[1];
;         if (nloc == 0u) { xcd_barrier_complete(bar, b.x, nloc, nx); b.st[0] = nloc; b.st[1] = nx; }
;         const unsigned old = xb_add(&bar[XB_XSUB(b.x)], 1u);
.LBB0_124:
	v_readlane_b32 s0, v253, 2
	s_mov_b32 s33, s94
	v_readlane_b32 s1, v253, 3
	s_mov_b32 s2, -1
	s_waitcnt lgkmcnt(0)
	s_barrier
	s_mov_b32 s3, s88
	s_waitcnt vmcnt(14)
	v_mbcnt_lo_u32_b32 v0, s2, 0
	v_mbcnt_hi_u32_b32 v0, s2, v0
	s_lshl_b32 s2, s97, 6
	s_waitcnt vmcnt(0)
	s_sub_i32 s2, 0, s2
	s_cmp_lg_u32 s97, 0
	s_cbranch_scc1 .Lwb_skip0
	buffer_wbl2 sc1
.Lwb_skip0:
	v_cmp_eq_u32_e32 vcc, s2, v0
	s_barrier
	s_and_saveexec_b64 s[2:3], vcc
	s_xor_b64 s[2:3], exec, s[2:3]
	s_cbranch_execz .LBB0_178
	s_add_i32 s4, 0, 0x20000
	v_mov_b32_e32 v0, s4
	s_waitcnt vmcnt(0) expcnt(0) lgkmcnt(0)
	ds_read_b32 v2, v0
	s_add_i32 s4, 0, 0x20004
	v_mov_b32_e32 v0, s4
	ds_read_b32 v0, v0
	s_waitcnt lgkmcnt(1)
	v_cmp_ne_u32_e32 vcc, 0, v2
	s_cbranch_vccnz .LBB0_141
	v_readlane_b32 s6, v253, 0
	v_readlane_b32 s7, v253, 1
	s_load_dwordx2 s[4:5], s[6:7], 0x4
	s_add_u32 s6, s0, 0x1000
	s_addc_u32 s7, s1, 0
	s_add_u32 s8, s0, 0x1100
	s_addc_u32 s9, s1, 0
	s_add_u32 s10, s0, 0x1200
	s_addc_u32 s11, s1, 0
	s_add_u32 s12, s0, 0x1300
	s_waitcnt lgkmcnt(0)
	s_mul_i32 s22, s4, s72
	s_addc_u32 s13, s1, 0
	s_mul_i32 s22, s22, s5
	s_mov_b32 s23, 1
	s_mov_b64 s[4:5], 0
	v_mov_b64_e32 v[0:1], s[0:1]
	v_mov_b64_e32 v[2:3], s[6:7]
	v_mov_b64_e32 v[4:5], s[8:9]
	v_mov_b64_e32 v[6:7], s[10:11]
	v_mov_b64_e32 v[8:9], s[12:13]
	s_branch .LBB0_129

; __device__ __forceinline__ void xcd_barrier(const XcdBarrier& b, bool t0) {
;     asm volatile("s_waitcnt vmcnt(0)" ::: "memory");
;     __syncthreads();
;     if (t0) {
.LBB0_181:
	v_readlane_b32 s0, v253, 2
	s_mov_b32 s33, s94
	v_readlane_b32 s1, v253, 3
	s_mov_b32 s39, s88
	v_mbcnt_lo_u32_b32 v0, s10, 0
	v_mbcnt_hi_u32_b32 v0, s10, v0
	s_lshl_b32 s2, s97, 6
	s_waitcnt vmcnt(0)
	s_sub_i32 s2, 0, s2
	s_cmp_lg_u32 s97, 0
	s_cbranch_scc1 .Lwb_skip1
	buffer_wbl2 sc1

; __device__ __forceinline__ unsigned xb_ld(unsigned* p)              { return __hip_atomic_load(p, __ATOMIC_RELAXED, __HIP_MEMORY_SCOPE_AGENT); }
; __device__ __forceinline__ unsigned xb_add(unsigned* p, unsigned v) { return __hip_atomic_fetch_add(p, v, __ATOMIC_RELAXED, __HIP_MEMORY_SCOPE_AGENT); }
; __device__ __forceinline__ void xcd_barrier_complete(unsigned* bar, unsigned x, unsigned& nloc, unsigned& nx) {
;     const unsigned G = gridDim.x * gridDim.y * gridDim.z;
;     unsigned sum, cnt, mine, sp = 0u;
;     for (;;) {
;         sum = 0u; cnt = 0u; mine = 0u;
; #pragma unroll
;         for (unsigned j = 0; j < 16; ++j) { const unsigned c = xb_ld(&bar[XB_XCNT(j)]); sum += c; cnt += (c > 0u) ? 1u : 0u; mine = (j == x) ? c : mine; }
; __device__ __forceinline__ void xcd_barrier(const XcdBarrier& b, bool t0) {
;     asm volatile("s_waitcnt vmcnt(0)" ::: "memory");
;     __syncthreads();
;     if (t0) {
;         unsigned* bar = b.bar;
;         __builtin_amdgcn_s_waitcnt(0);
;         unsigned nloc = b.st[0], nx = b.st[1];
;         if (nloc == 0u) { xcd_barrier_complete(bar, b.x, nloc, nx); b.st[0] = nloc; b.st[1] = nx; }
;         const unsigned old = xb_add(&bar[XB_XSUB(b.x)], 1u);
.LBB0_274:
	v_readlane_b32 s36, v253, 2
	v_readlane_b32 s37, v253, 3
	s_mov_b32 s0, s94
	s_mov_b32 s1, -1
	v_readlane_b32 s2, v253, 29
	s_waitcnt lgkmcnt(0)
	v_mbcnt_lo_u32_b32 v0, s1, 0
	v_mbcnt_hi_u32_b32 v0, s1, v0
	s_mov_b32 s33, s2
	s_lshl_b32 s1, s97, 6
	s_waitcnt vmcnt(0)
	s_sub_i32 s1, 0, s1
	v_readlane_b32 s3, v253, 30
	s_cmp_lg_u32 s97, 0
	s_cbranch_scc1 .Lwb_skip2
	buffer_wbl2 sc1
.Lwb_skip2:
	v_cmp_eq_u32_e32 vcc, s1, v0
	s_waitcnt vmcnt(0)
	s_barrier
	s_and_saveexec_b64 s[2:3], vcc
	s_xor_b64 s[2:3], exec, s[2:3]
	s_cbranch_execz .LBB0_319
	s_add_i32 s1, 0, 0x20000
	v_mov_b32_e32 v0, s1
	s_waitcnt vmcnt(0) expcnt(0) lgkmcnt(0)
	ds_read_b32 v2, v0
	v_mov_b32_e32 v0, s73
	ds_read_b32 v0, v0
	s_waitcnt lgkmcnt(1)
	v_cmp_ne_u32_e32 vcc, 0, v2
	s_cbranch_vccnz .LBB0_289
	v_readlane_b32 s4, v253, 0
	v_readlane_b32 s5, v253, 1
	s_load_dwordx2 s[8:9], s[4:5], 0x4
	s_add_u32 s4, s36, 0x1000
	s_addc_u32 s5, s37, 0
	s_add_u32 s6, s36, 0x1100
	s_addc_u32 s7, s37, 0
	s_waitcnt lgkmcnt(0)
	s_mul_i32 s30, s8, s72
	s_add_u32 s8, s36, 0x1200
	s_mul_i32 s30, s30, s9
	s_addc_u32 s9, s37, 0
	s_add_u32 s10, s36, 0x1300
	s_addc_u32 s11, s37, 0
	s_mov_b32 s31, 1
	s_mov_b64 s[12:13], 0
	s_branch .LBB0_279

; __device__ __forceinline__ unsigned xb_ld(unsigned* p)              { return __hip_atomic_load(p, __ATOMIC_RELAXED, __HIP_MEMORY_SCOPE_AGENT); }
; __device__ __forceinline__ unsigned xb_add(unsigned* p, unsigned v) { return __hip_atomic_fetch_add(p, v, __ATOMIC_RELAXED, __HIP_MEMORY_SCOPE_AGENT); }
; __device__ __forceinline__ void xcd_barrier_complete(unsigned* bar, unsigned x, unsigned& nloc, unsigned& nx) {
;     const unsigned G = gridDim.x * gridDim.y * gridDim.z;
;     unsigned sum, cnt, mine, sp = 0u;
;     for (;;) {
;         sum = 0u; cnt = 0u; mine = 0u;
; #pragma unroll
;         for (unsigned j = 0; j < 16; ++j) { const unsigned c = xb_ld(&bar[XB_XCNT(j)]); sum += c; cnt += (c > 0u) ? 1u : 0u; mine = (j == x) ? c : mine; }
; __device__ __forceinline__ void xcd_barrier(const XcdBarrier& b, bool t0) {
;     asm volatile("s_waitcnt vmcnt(0)" ::: "memory");
;     __syncthreads();
;     if (t0) {
;         unsigned* bar = b.bar;
;         __builtin_amdgcn_s_waitcnt(0);
;         unsigned nloc = b.st[0], nx = b.st[1];
;         if (nloc == 0u) { xcd_barrier_complete(bar, b.x, nloc, nx); b.st[0] = nloc; b.st[1] = nx; }
;         const unsigned old = xb_add(&bar[XB_XSUB(b.x)], 1u);
.LBB0_350:
	v_readlane_b32 s36, v253, 2
	s_mov_b32 s0, s94
	v_readlane_b32 s37, v253, 3
	s_mov_b32 s1, -1
	v_readlane_b32 s2, v253, 29
	v_mbcnt_lo_u32_b32 v0, s1, 0
	v_mbcnt_hi_u32_b32 v0, s1, v0
	s_lshl_b32 s1, s97, 6
	s_waitcnt vmcnt(0)
	s_sub_i32 s1, 0, s1
	v_readlane_b32 s3, v253, 30
	s_cmp_lg_u32 s97, 0
	s_cbranch_scc1 .Lwb_skip3
	buffer_wbl2 sc1
.Lwb_skip3:
	v_cmp_eq_u32_e32 vcc, s1, v0
	s_waitcnt vmcnt(0) lgkmcnt(0)
	s_barrier
	s_and_saveexec_b64 s[2:3], vcc
	s_xor_b64 s[2:3], exec, s[2:3]
	s_cbranch_execz .LBB0_395
	s_add_i32 s1, 0, 0x20000
	v_mov_b32_e32 v0, s1
	s_waitcnt vmcnt(0) expcnt(0) lgkmcnt(0)
	ds_read_b32 v2, v0
	v_mov_b32_e32 v0, s73
	ds_read_b32 v0, v0
	s_waitcnt lgkmcnt(1)
	v_cmp_ne_u32_e32 vcc, 0, v2
	s_cbranch_vccnz .LBB0_365
	v_readlane_b32 s4, v253, 0
	v_readlane_b32 s5, v253, 1
	s_load_dwordx2 s[8:9], s[4:5], 0x4
	s_add_u32 s4, s36, 0x1000
	s_addc_u32 s5, s37, 0
	s_add_u32 s6, s36, 0x1100
	s_addc_u32 s7, s37, 0
	s_waitcnt lgkmcnt(0)
	s_mul_i32 s30, s8, s72
	s_add_u32 s8, s36, 0x1200
	s_mul_i32 s30, s30, s9
	s_addc_u32 s9, s37, 0
	s_add_u32 s10, s36, 0x1300
	s_addc_u32 s11, s37, 0
	s_mov_b32 s31, 1
	s_mov_b64 s[12:13], 0
	s_branch .LBB0_355

; __device__ __forceinline__ unsigned xb_ld(unsigned* p)              { return __hip_atomic_load(p, __ATOMIC_RELAXED, __HIP_MEMORY_SCOPE_AGENT); }
; __device__ __forceinline__ unsigned xb_add(unsigned* p, unsigned v) { return __hip_atomic_fetch_add(p, v, __ATOMIC_RELAXED, __HIP_MEMORY_SCOPE_AGENT); }
; __device__ __forceinline__ void xcd_barrier_complete(unsigned* bar, unsigned x, unsigned& nloc, unsigned& nx) {
;     const unsigned G = gridDim.x * gridDim.y * gridDim.z;
;     unsigned sum, cnt, mine, sp = 0u;
;     for (;;) {
;         sum = 0u; cnt = 0u; mine = 0u;
; #pragma unroll
;         for (unsigned j = 0; j < 16; ++j) { const unsigned c = xb_ld(&bar[XB_XCNT(j)]); sum += c; cnt += (c > 0u) ? 1u : 0u; mine = (j == x) ? c : mine; }
; __device__ __forceinline__ void xcd_barrier(const XcdBarrier& b, bool t0) {
;     asm volatile("s_waitcnt vmcnt(0)" ::: "memory");
;     __syncthreads();
;     if (t0) {
;         unsigned* bar = b.bar;
;         __builtin_amdgcn_s_waitcnt(0);
;         unsigned nloc = b.st[0], nx = b.st[1];
;         if (nloc == 0u) { xcd_barrier_complete(bar, b.x, nloc, nx); b.st[0] = nloc; b.st[1] = nx; }
;         const unsigned old = xb_add(&bar[XB_XSUB(b.x)], 1u);
.LBB0_715:
	v_readlane_b32 s42, v253, 2
	s_mov_b32 s0, s94
	v_readlane_b32 s43, v253, 3
	s_mov_b32 s1, -1
	s_waitcnt lgkmcnt(0)
	s_barrier
	v_readlane_b32 s2, v253, 29
	v_mbcnt_lo_u32_b32 v0, s1, 0
	v_mbcnt_hi_u32_b32 v0, s1, v0
	s_mov_b32 s36, s2
	s_lshl_b32 s1, s97, 6
	s_waitcnt vmcnt(0)
	s_sub_i32 s1, 0, s1
	v_readlane_b32 s3, v253, 30
	s_cmp_lg_u32 s97, 0
	s_cbranch_scc1 .Lwb_skip4
	buffer_wbl2 sc1
.Lwb_skip4:
	v_cmp_eq_u32_e32 vcc, s1, v0
	s_barrier
	s_and_saveexec_b64 s[2:3], vcc
	s_xor_b64 s[2:3], exec, s[2:3]
	v_readlane_b32 s38, v255, 7
	v_readlane_b32 s48, v253, 57
	s_movk_i32 s63, 0x500
	v_readlane_b32 s73, v255, 13
	s_mov_b32 s51, 0x800000
	v_readlane_b32 s39, v255, 8
	s_cbranch_execz .LBB0_760
	s_add_i32 s1, 0, 0x20000
	v_mov_b32_e32 v0, s1
	s_waitcnt vmcnt(0) expcnt(0) lgkmcnt(0)
	ds_read_b32 v2, v0
	v_mov_b32_e32 v0, s73
	ds_read_b32 v0, v0
	s_waitcnt lgkmcnt(1)
	v_cmp_ne_u32_e32 vcc, 0, v2
	s_cbranch_vccnz .LBB0_730
	v_readlane_b32 s4, v253, 0
	v_readlane_b32 s5, v253, 1
	s_load_dwordx2 s[8:9], s[4:5], 0x4
	s_add_u32 s4, s42, 0x1000
	s_addc_u32 s5, s43, 0
	s_add_u32 s6, s42, 0x1100
	s_addc_u32 s7, s43, 0
	s_waitcnt lgkmcnt(0)
	s_mul_i32 s30, s8, s72
	s_add_u32 s8, s42, 0x1200
	s_mul_i32 s30, s30, s9
	s_addc_u32 s9, s43, 0
	s_add_u32 s10, s42, 0x1300
	s_addc_u32 s11, s43, 0
	s_mov_b32 s31, 1
	s_mov_b64 s[12:13], 0
	s_branch .LBB0_720

; __device__ __forceinline__ unsigned xb_ld(unsigned* p)              { return __hip_atomic_load(p, __ATOMIC_RELAXED, __HIP_MEMORY_SCOPE_AGENT); }
; __device__ __forceinline__ unsigned xb_add(unsigned* p, unsigned v) { return __hip_atomic_fetch_add(p, v, __ATOMIC_RELAXED, __HIP_MEMORY_SCOPE_AGENT); }
; __device__ __forceinline__ void xcd_barrier_complete(unsigned* bar, unsigned x, unsigned& nloc, unsigned& nx) {
;     const unsigned G = gridDim.x * gridDim.y * gridDim.z;
;     unsigned sum, cnt, mine, sp = 0u;
;     for (;;) {
;         sum = 0u; cnt = 0u; mine = 0u;
; #pragma unroll
;         for (unsigned j = 0; j < 16; ++j) { const unsigned c = xb_ld(&bar[XB_XCNT(j)]); sum += c; cnt += (c > 0u) ? 1u : 0u; mine = (j == x) ? c : mine; }
; __device__ __forceinline__ void xcd_barrier(const XcdBarrier& b, bool t0) {
;     asm volatile("s_waitcnt vmcnt(0)" ::: "memory");
;     __syncthreads();
;     if (t0) {
;         unsigned* bar = b.bar;
;         __builtin_amdgcn_s_waitcnt(0);
;         unsigned nloc = b.st[0], nx = b.st[1];
;         if (nloc == 0u) { xcd_barrier_complete(bar, b.x, nloc, nx); b.st[0] = nloc; b.st[1] = nx; }
;         const unsigned old = xb_add(&bar[XB_XSUB(b.x)], 1u);
.LBB0_776:
	v_readlane_b32 s42, v253, 2
	s_mov_b32 s0, s94
	v_readlane_b32 s43, v253, 3
	s_mov_b32 s1, -1
	v_readlane_b32 s2, v253, 29
	v_mbcnt_lo_u32_b32 v0, s1, 0
	v_mbcnt_hi_u32_b32 v0, s1, v0
	s_mov_b32 s33, s2
	s_lshl_b32 s1, s97, 6
	s_waitcnt vmcnt(0)
	s_sub_i32 s1, 0, s1
	v_readlane_b32 s3, v253, 30
	s_cmp_lg_u32 s97, 0
	s_cbranch_scc1 .Lwb_skip5
	buffer_wbl2 sc1
.Lwb_skip5:
	v_cmp_eq_u32_e32 vcc, s1, v0
	s_waitcnt vmcnt(0)
	s_barrier
	s_and_saveexec_b64 s[2:3], vcc
	s_xor_b64 s[2:3], exec, s[2:3]
	s_cbranch_execz .LBB0_821
	s_add_i32 s1, 0, 0x20000
	v_mov_b32_e32 v0, s1
	s_waitcnt vmcnt(0) expcnt(0) lgkmcnt(0)
	ds_read_b32 v2, v0
	v_mov_b32_e32 v0, s73
	ds_read_b32 v0, v0
	s_waitcnt lgkmcnt(1)
	v_cmp_ne_u32_e32 vcc, 0, v2
	s_cbranch_vccnz .LBB0_791
	v_readlane_b32 s4, v253, 0
	v_readlane_b32 s5, v253, 1
	s_load_dwordx2 s[8:9], s[4:5], 0x4
	s_add_u32 s4, s42, 0x1000
	s_addc_u32 s5, s43, 0
	s_add_u32 s6, s42, 0x1100
	s_addc_u32 s7, s43, 0
	s_waitcnt lgkmcnt(0)
	s_mul_i32 s30, s8, s72
	s_add_u32 s8, s42, 0x1200
	s_mul_i32 s30, s30, s9
	s_addc_u32 s9, s43, 0
	s_add_u32 s10, s42, 0x1300
	s_addc_u32 s11, s43, 0
	s_mov_b32 s31, 1
	s_mov_b64 s[12:13], 0
	s_branch .LBB0_781

; __device__ __forceinline__ void xcd_barrier(const XcdBarrier& b, bool t0) {
;     asm volatile("s_waitcnt vmcnt(0)" ::: "memory");
;     __syncthreads();
;     if (t0) {
.LBB0_841:
	v_readlane_b32 s42, v253, 2
	v_readlane_b32 s43, v253, 3
	s_mov_b32 s0, s94
	s_mov_b32 s1, -1
	v_readlane_b32 s2, v253, 29
	v_mbcnt_lo_u32_b32 v0, s1, 0
	v_mbcnt_hi_u32_b32 v0, s1, v0
	s_mov_b32 s36, s2
	s_lshl_b32 s1, s97, 6
	s_waitcnt vmcnt(0)
	s_sub_i32 s1, 0, s1
	v_readlane_b32 s3, v253, 30
	s_cmp_lg_u32 s97, 0
	s_cbranch_scc1 .Lwb_skip6
	buffer_wbl2 sc1

; __device__ __forceinline__ unsigned xb_add(unsigned* p, unsigned v) { return __hip_atomic_fetch_add(p, v, __ATOMIC_RELAXED, __HIP_MEMORY_SCOPE_AGENT); }
; __device__ __forceinline__ void xcd_barrier_complete(unsigned* bar, unsigned x, unsigned& nloc, unsigned& nx) {
;     const unsigned G = gridDim.x * gridDim.y * gridDim.z;
;     unsigned sum, cnt, mine, sp = 0u;
; __device__ __forceinline__ void xcd_barrier(const XcdBarrier& b, bool t0) {
;     ...
;     __syncthreads();
;     if (t0) {
;         unsigned* bar = b.bar;
;         __builtin_amdgcn_s_waitcnt(0);
;         unsigned nloc = b.st[0], nx = b.st[1];
;         if (nloc == 0u) { xcd_barrier_complete(bar, b.x, nloc, nx); b.st[0] = nloc; b.st[1] = nx; }
;         const unsigned old = xb_add(&bar[XB_XSUB(b.x)], 1u);
.Lwb_skip7:
	v_cmp_eq_u32_e32 vcc, s1, v0
	s_barrier
	s_and_saveexec_b64 s[2:3], vcc
	s_xor_b64 s[2:3], exec, s[2:3]
	s_cbranch_execz .LBB0_959
	s_add_i32 s1, 0, 0x20000
	v_mov_b32_e32 v0, s1
	s_waitcnt vmcnt(0) expcnt(0) lgkmcnt(0)
	ds_read_b32 v2, v0
	v_mov_b32_e32 v0, s73
	ds_read_b32 v0, v0
	s_waitcnt lgkmcnt(1)
	v_cmp_ne_u32_e32 vcc, 0, v2
	s_cbranch_vccnz .LBB0_929
	v_readlane_b32 s4, v253, 0
	v_readlane_b32 s5, v253, 1
	s_load_dwordx2 s[8:9], s[4:5], 0x4
	s_add_u32 s4, s42, 0x1000
	s_addc_u32 s5, s43, 0
	s_add_u32 s6, s42, 0x1100
	s_addc_u32 s7, s43, 0
	s_waitcnt lgkmcnt(0)
	s_mul_i32 s30, s8, s72
	s_add_u32 s8, s42, 0x1200
	s_mul_i32 s30, s30, s9
	s_addc_u32 s9, s43, 0
	s_add_u32 s10, s42, 0x1300
	s_addc_u32 s11, s43, 0
	s_mov_b32 s31, 1
	s_mov_b64 s[12:13], 0
	s_branch .LBB0_919

; __device__ __forceinline__ unsigned xb_ld(unsigned* p)              { return __hip_atomic_load(p, __ATOMIC_RELAXED, __HIP_MEMORY_SCOPE_AGENT); }
; __device__ __forceinline__ unsigned xb_add(unsigned* p, unsigned v) { return __hip_atomic_fetch_add(p, v, __ATOMIC_RELAXED, __HIP_MEMORY_SCOPE_AGENT); }
; __device__ __forceinline__ void xcd_barrier_complete(unsigned* bar, unsigned x, unsigned& nloc, unsigned& nx) {
;     const unsigned G = gridDim.x * gridDim.y * gridDim.z;
;     unsigned sum, cnt, mine, sp = 0u;
;     for (;;) {
;         sum = 0u; cnt = 0u; mine = 0u;
; #pragma unroll
;         for (unsigned j = 0; j < 16; ++j) { const unsigned c = xb_ld(&bar[XB_XCNT(j)]); sum += c; cnt += (c > 0u) ? 1u : 0u; mine = (j == x) ? c : mine; }
; __device__ __forceinline__ void xcd_barrier(const XcdBarrier& b, bool t0) {
;     asm volatile("s_waitcnt vmcnt(0)" ::: "memory");
;     __syncthreads();
;     if (t0) {
;         unsigned* bar = b.bar;
;         __builtin_amdgcn_s_waitcnt(0);
;         unsigned nloc = b.st[0], nx = b.st[1];
;         if (nloc == 0u) { xcd_barrier_complete(bar, b.x, nloc, nx); b.st[0] = nloc; b.st[1] = nx; }
;         const unsigned old = xb_add(&bar[XB_XSUB(b.x)], 1u);
.LBB0_979:
	v_readlane_b32 s36, v253, 2
	v_readlane_b32 s37, v253, 3
	s_mov_b32 s0, s94
	s_mov_b32 s1, -1
	v_readlane_b32 s2, v253, 29
	v_mbcnt_lo_u32_b32 v0, s1, 0
	v_mbcnt_hi_u32_b32 v0, s1, v0
	s_lshl_b32 s1, s97, 6
	s_waitcnt vmcnt(0)
	s_sub_i32 s1, 0, s1
	v_readlane_b32 s3, v253, 30
	s_cmp_lg_u32 s97, 0
	s_cbranch_scc1 .Lwb_skip8
	buffer_wbl2 sc1
.Lwb_skip8:
	v_cmp_eq_u32_e32 vcc, s1, v0
	s_waitcnt vmcnt(0)
	s_barrier
	s_and_saveexec_b64 s[2:3], vcc
	v_readlane_b32 s44, v255, 20
	s_xor_b64 s[2:3], exec, s[2:3]
	v_readlane_b32 s45, v255, 21
	s_cbranch_execz .LBB0_1024
	s_add_i32 s1, 0, 0x20000
	v_mov_b32_e32 v0, s1
	s_waitcnt vmcnt(0) expcnt(0) lgkmcnt(0)
	ds_read_b32 v2, v0
	v_mov_b32_e32 v0, s73
	ds_read_b32 v0, v0
	s_waitcnt lgkmcnt(1)
	v_cmp_ne_u32_e32 vcc, 0, v2
	s_cbranch_vccnz .LBB0_994
	v_readlane_b32 s4, v253, 0
	v_readlane_b32 s5, v253, 1
	s_load_dwordx2 s[8:9], s[4:5], 0x4
	s_add_u32 s4, s36, 0x1000
	s_addc_u32 s5, s37, 0
	s_add_u32 s6, s36, 0x1100
	s_addc_u32 s7, s37, 0
	s_waitcnt lgkmcnt(0)
	s_mul_i32 s30, s8, s72
	s_add_u32 s8, s36, 0x1200
	s_mul_i32 s30, s30, s9
	s_addc_u32 s9, s37, 0
	s_add_u32 s10, s36, 0x1300
	s_addc_u32 s11, s37, 0
	s_mov_b32 s31, 1
	s_mov_b64 s[12:13], 0
	s_branch .LBB0_984

; __device__ __forceinline__ unsigned xb_ld(unsigned* p)              { return __hip_atomic_load(p, __ATOMIC_RELAXED, __HIP_MEMORY_SCOPE_AGENT); }
; __device__ __forceinline__ unsigned xb_add(unsigned* p, unsigned v) { return __hip_atomic_fetch_add(p, v, __ATOMIC_RELAXED, __HIP_MEMORY_SCOPE_AGENT); }
; __device__ __forceinline__ void xcd_barrier_complete(unsigned* bar, unsigned x, unsigned& nloc, unsigned& nx) {
;     const unsigned G = gridDim.x * gridDim.y * gridDim.z;
;     unsigned sum, cnt, mine, sp = 0u;
;     for (;;) {
;         sum = 0u; cnt = 0u; mine = 0u;
; #pragma unroll
;         for (unsigned j = 0; j < 16; ++j) { const unsigned c = xb_ld(&bar[XB_XCNT(j)]); sum += c; cnt += (c > 0u) ? 1u : 0u; mine = (j == x) ? c : mine; }
; __device__ __forceinline__ void xcd_barrier(const XcdBarrier& b, bool t0) {
;     asm volatile("s_waitcnt vmcnt(0)" ::: "memory");
;     __syncthreads();
;     if (t0) {
;         unsigned* bar = b.bar;
;         __builtin_amdgcn_s_waitcnt(0);
;         unsigned nloc = b.st[0], nx = b.st[1];
;         if (nloc == 0u) { xcd_barrier_complete(bar, b.x, nloc, nx); b.st[0] = nloc; b.st[1] = nx; }
;         const unsigned old = xb_add(&bar[XB_XSUB(b.x)], 1u);
.LBB0_1128:
	v_readlane_b32 s2, v253, 2
	s_mov_b32 s0, s94
	v_readlane_b32 s3, v253, 3
	s_mov_b32 s1, -1
	s_barrier
	v_readlane_b32 s4, v253, 29
	v_mbcnt_lo_u32_b32 v0, s1, 0
	v_mbcnt_hi_u32_b32 v0, s1, v0
	s_mov_b32 s33, s4
	s_waitcnt vmcnt(0)
	v_readlane_b32 s5, v253, 30
	v_lshl_add_u32 v4, s97, 6, v0
	s_cmp_lg_u32 s97, 0
	s_cbranch_scc1 .Lwb_skip9
	buffer_wbl2 sc1
.Lwb_skip9:
	v_cmp_eq_u32_e64 s[4:5], 0, v4
	s_barrier
	s_and_saveexec_b64 s[56:57], s[4:5]
	s_cbranch_execz .LBB0_1172
	s_add_i32 s1, 0, 0x20000
	v_mov_b32_e32 v0, s1
	s_waitcnt vmcnt(0) expcnt(0) lgkmcnt(0)
	ds_read_b32 v2, v0
	v_mov_b32_e32 v0, s73
	ds_read_b32 v0, v0
	s_waitcnt lgkmcnt(1)
	v_cmp_ne_u32_e32 vcc, 0, v2
	s_cbranch_vccnz .LBB0_1143
	v_readlane_b32 s6, v253, 0
	v_readlane_b32 s7, v253, 1
	s_load_dwordx2 s[10:11], s[6:7], 0x4
	s_add_u32 s6, s2, 0x1000
	s_addc_u32 s7, s3, 0
	s_add_u32 s8, s2, 0x1100
	s_addc_u32 s9, s3, 0
	s_waitcnt lgkmcnt(0)
	s_mul_i32 s34, s10, s72
	s_add_u32 s10, s2, 0x1200
	s_mul_i32 s34, s34, s11
	s_addc_u32 s11, s3, 0
	s_add_u32 s12, s2, 0x1300
	s_addc_u32 s13, s3, 0
	s_mov_b32 s35, 1
	s_mov_b64 s[14:15], 0
	s_branch .LBB0_1133

; __device__ __forceinline__ void xcd_barrier(const XcdBarrier& b, bool t0) {
;     asm volatile("s_waitcnt vmcnt(0)" ::: "memory");
;     __syncthreads();
;     if (t0) {
.LBB0_1242:
	v_readlane_b32 s36, v253, 2
	s_mov_b32 s0, s94
	v_readlane_b32 s37, v253, 3
	s_mov_b32 s1, -1
	v_readlane_b32 s2, v253, 29
	v_mbcnt_lo_u32_b32 v0, s1, 0
	v_mbcnt_hi_u32_b32 v0, s1, v0
	s_mov_b32 s33, s2
	s_lshl_b32 s1, s97, 6
	s_waitcnt vmcnt(0)
	s_sub_i32 s1, 0, s1
	v_readlane_b32 s3, v253, 30
	s_cmp_lg_u32 s97, 0
	s_cbranch_scc1 .Lwb_skip10
	buffer_wbl2 sc1

; __device__ __forceinline__ unsigned xb_add(unsigned* p, unsigned v) { return __hip_atomic_fetch_add(p, v, __ATOMIC_RELAXED, __HIP_MEMORY_SCOPE_AGENT); }
; __device__ __forceinline__ void xcd_barrier_complete(unsigned* bar, unsigned x, unsigned& nloc, unsigned& nx) {
;     const unsigned G = gridDim.x * gridDim.y * gridDim.z;
;     unsigned sum, cnt, mine, sp = 0u;
; __device__ __forceinline__ void xcd_barrier(const XcdBarrier& b, bool t0) {
;     ...
;     __syncthreads();
;     if (t0) {
;         unsigned* bar = b.bar;
;         __builtin_amdgcn_s_waitcnt(0);
;         unsigned nloc = b.st[0], nx = b.st[1];
;         if (nloc == 0u) { xcd_barrier_complete(bar, b.x, nloc, nx); b.st[0] = nloc; b.st[1] = nx; }
;         const unsigned old = xb_add(&bar[XB_XSUB(b.x)], 1u);
.Lwb_skip11:
	v_cmp_eq_u32_e32 vcc, s1, v0
	s_waitcnt vmcnt(0) lgkmcnt(0)
	s_barrier
	s_and_saveexec_b64 s[2:3], vcc
	v_readlane_b32 s70, v253, 6
	s_xor_b64 s[2:3], exec, s[2:3]
	v_readlane_b32 s71, v253, 7
	s_cbranch_execz .LBB0_1397
	s_add_i32 s1, 0, 0x20000
	v_mov_b32_e32 v0, s1
	s_waitcnt vmcnt(0) expcnt(0) lgkmcnt(0)
	ds_read_b32 v2, v0
	v_mov_b32_e32 v0, s73
	ds_read_b32 v0, v0
	s_waitcnt lgkmcnt(1)
	v_cmp_ne_u32_e32 vcc, 0, v2
	s_cbranch_vccnz .LBB0_1367
	v_readlane_b32 s4, v253, 0
	v_readlane_b32 s5, v253, 1
	s_load_dwordx2 s[8:9], s[4:5], 0x4
	s_add_u32 s4, s36, 0x1000
	s_addc_u32 s5, s37, 0
	s_add_u32 s6, s36, 0x1100
	s_addc_u32 s7, s37, 0
	s_waitcnt lgkmcnt(0)
	s_mul_i32 s30, s8, s72
	s_add_u32 s8, s36, 0x1200
	s_mul_i32 s30, s30, s9
	s_addc_u32 s9, s37, 0
	s_add_u32 s10, s36, 0x1300
	s_addc_u32 s11, s37, 0
	s_mov_b32 s31, 1
	s_mov_b64 s[12:13], 0
	s_branch .LBB0_1357

; __device__ __forceinline__ void xcd_barrier(const XcdBarrier& b, bool t0) {
;     asm volatile("s_waitcnt vmcnt(0)" ::: "memory");
;     __syncthreads();
;     if (t0) {
.LBB0_1438:
	v_readlane_b32 s2, v253, 2
	s_mov_b32 s0, s94
	v_readlane_b32 s3, v253, 3
	s_mov_b32 s1, -1
	v_readlane_b32 s4, v253, 29
	v_mbcnt_lo_u32_b32 v0, s1, 0
	v_mbcnt_hi_u32_b32 v0, s1, v0
	s_mov_b32 s39, s4
	s_lshl_b32 s1, s97, 6
	s_waitcnt vmcnt(0)
	s_sub_i32 s1, 0, s1
	s_cmp_lg_u32 s97, 0
	s_cbranch_scc1 .Lwb_skip12
	buffer_wbl2 sc1
.Lwb_skip12:
	v_cmp_eq_u32_e32 vcc, s1, v0
	v_readlane_b32 s5, v253, 30
	s_barrier
	s_and_saveexec_b64 s[36:37], vcc
	s_cbranch_execnz .LBB0_1439
	s_getpc_b64 s[98:99]
